# v99 + k9 start: the three slot-table loads issued back to back (LDS writes deferred to one wait); k8: token expert/rank loads hoisted above the histogram phase
# baseline (speedup 1.0000x reference)
.LBB0_1132:
	v_mov_b32_e32 v3, v0
	s_waitcnt vmcnt(0)
	v_ashrrev_i32_e32 v89, 31, v2
	v_mov_b32_e32 v88, v2
	v_lshlrev_b64 v[90:91], 2, v[88:89]
	v_lshl_add_u64 v[92:93], s[46:47], 0, v[90:91]
	global_load_dword v86, v[92:93], off
	v_lshl_add_u64 v[92:93], s[44:45], 0, v[90:91]
	global_load_dword v87, v[92:93], off
	v_ashrrev_i32_e32 v4, 1, v3
	v_and_b32_e32 v5, 31, v3
	v_and_b32_e32 v8, -16, v4
	v_lshl_or_b32 v6, v8, 5, v5
	v_ashrrev_i32_e32 v7, 31, v6
	v_lshl_add_u64 v[6:7], v[6:7], 2, s[48:49]
	s_barrier
	global_load_dword v70, v[6:7], off
	global_load_dword v71, v[6:7], off offset:128
	global_load_dword v72, v[6:7], off offset:256
	global_load_dword v73, v[6:7], off offset:384
	global_load_dword v74, v[6:7], off offset:512
	global_load_dword v75, v[6:7], off offset:640
	global_load_dword v76, v[6:7], off offset:768
	global_load_dword v77, v[6:7], off offset:896
	global_load_dword v78, v[6:7], off offset:1024
	global_load_dword v79, v[6:7], off offset:1152
	global_load_dword v80, v[6:7], off offset:1280
	global_load_dword v81, v[6:7], off offset:1408
	global_load_dword v82, v[6:7], off offset:1536
	global_load_dword v83, v[6:7], off offset:1664
	global_load_dword v84, v[6:7], off offset:1792
	global_load_dword v85, v[6:7], off offset:1920
	v_lshlrev_b32_e32 v5, 2, v5
	v_mov_b32_e32 v10, 0
	s_waitcnt vmcnt(0)
	v_add_u32_e32 v9, v70, v71
	v_add3_u32 v9, v9, v72, v73
	v_add3_u32 v9, v9, v74, v75
	v_add3_u32 v9, v9, v76, v77
	v_add3_u32 v9, v9, v78, v79
	v_add3_u32 v9, v9, v80, v81
	v_add3_u32 v9, v9, v82, v83
	v_add3_u32 v9, v9, v84, v85
	v_or_b32_e32 v11, 0, v8
	v_cmp_gt_i32_e64 s[38:39], s2, v11
	s_nop 1
	v_cndmask_b32_e64 v12, 0, v70, s[38:39]
	v_add_u32_e32 v10, v10, v12
	v_or_b32_e32 v11, 1, v8
	v_cmp_gt_i32_e64 s[38:39], s2, v11
	s_nop 1
	v_cndmask_b32_e64 v12, 0, v71, s[38:39]
	v_add_u32_e32 v10, v10, v12
	v_or_b32_e32 v11, 2, v8
	v_cmp_gt_i32_e64 s[38:39], s2, v11
	s_nop 1
	v_cndmask_b32_e64 v12, 0, v72, s[38:39]
	v_add_u32_e32 v10, v10, v12
	v_or_b32_e32 v11, 3, v8
	v_cmp_gt_i32_e64 s[38:39], s2, v11
	s_nop 1
	v_cndmask_b32_e64 v12, 0, v73, s[38:39]
	v_add_u32_e32 v10, v10, v12
	v_or_b32_e32 v11, 4, v8
	v_cmp_gt_i32_e64 s[38:39], s2, v11
	s_nop 1
	v_cndmask_b32_e64 v12, 0, v74, s[38:39]
	v_add_u32_e32 v10, v10, v12
	v_or_b32_e32 v11, 5, v8
	v_cmp_gt_i32_e64 s[38:39], s2, v11
	s_nop 1
	v_cndmask_b32_e64 v12, 0, v75, s[38:39]
	v_add_u32_e32 v10, v10, v12
	v_or_b32_e32 v11, 6, v8
	v_cmp_gt_i32_e64 s[38:39], s2, v11
	s_nop 1
	v_cndmask_b32_e64 v12, 0, v76, s[38:39]
	v_add_u32_e32 v10, v10, v12
	v_or_b32_e32 v11, 7, v8
	v_cmp_gt_i32_e64 s[38:39], s2, v11
	s_nop 1
	v_cndmask_b32_e64 v12, 0, v77, s[38:39]
	v_add_u32_e32 v10, v10, v12
	v_or_b32_e32 v11, 8, v8
	v_cmp_gt_i32_e64 s[38:39], s2, v11
	s_nop 1
	v_cndmask_b32_e64 v12, 0, v78, s[38:39]
	v_add_u32_e32 v10, v10, v12
	v_or_b32_e32 v11, 9, v8
	v_cmp_gt_i32_e64 s[38:39], s2, v11
	s_nop 1
	v_cndmask_b32_e64 v12, 0, v79, s[38:39]
	v_add_u32_e32 v10, v10, v12
	v_or_b32_e32 v11, 10, v8
	v_cmp_gt_i32_e64 s[38:39], s2, v11
	s_nop 1
	v_cndmask_b32_e64 v12, 0, v80, s[38:39]
	v_add_u32_e32 v10, v10, v12
	v_or_b32_e32 v11, 11, v8
	v_cmp_gt_i32_e64 s[38:39], s2, v11
	s_nop 1
	v_cndmask_b32_e64 v12, 0, v81, s[38:39]
	v_add_u32_e32 v10, v10, v12
	v_or_b32_e32 v11, 12, v8
	v_cmp_gt_i32_e64 s[38:39], s2, v11
	s_nop 1
	v_cndmask_b32_e64 v12, 0, v82, s[38:39]
	v_add_u32_e32 v10, v10, v12
	v_or_b32_e32 v11, 13, v8
	v_cmp_gt_i32_e64 s[38:39], s2, v11
	s_nop 1
	v_cndmask_b32_e64 v12, 0, v83, s[38:39]
	v_add_u32_e32 v10, v10, v12
	v_or_b32_e32 v11, 14, v8
	v_cmp_gt_i32_e64 s[38:39], s2, v11
	s_nop 1
	v_cndmask_b32_e64 v12, 0, v84, s[38:39]
	v_add_u32_e32 v10, v10, v12
	v_or_b32_e32 v11, 15, v8
	v_cmp_gt_i32_e64 s[38:39], s2, v11
	s_nop 1
	v_cndmask_b32_e64 v12, 0, v85, s[38:39]
	v_add_u32_e32 v10, v10, v12
	v_mov_b32_e32 v7, v9
	v_mov_b32_e32 v6, v10
	v_and_b32_e32 v8, 0x3fffffe0, v3
	v_lshl_add_u32 v4, v3, 2, 0
	ds_write_b32 v4, v7
	v_lshlrev_b32_e32 v7, 2, v8
	v_add3_u32 v5, 0, v7, v5
	v_cmp_gt_i32_e64 s[38:39], 32, v3
	ds_write_b32 v5, v6 offset:2048
	s_waitcnt lgkmcnt(0)
	s_barrier
	s_and_saveexec_b64 s[36:37], s[38:39]
	s_cbranch_execz .LBB0_1135
	v_add_u32_e32 v5, 0x800, v4
	ds_read2_b32 v[8:9], v5 offset1:32
	ds_read2_b32 v[6:7], v4 offset1:32
	v_add_u32_e32 v23, 0xc00, v4
	v_add_u32_e32 v22, 0x400, v4
	s_movk_i32 s3, 0xff
	s_waitcnt lgkmcnt(1)
	v_add_u32_e32 v12, v9, v8
	ds_read2_b32 v[8:9], v4 offset0:64 offset1:96
	ds_read2_b32 v[10:11], v5 offset0:64 offset1:96
	s_waitcnt lgkmcnt(0)
	v_add3_u32 v14, v12, v10, v11
	ds_read2_b32 v[10:11], v4 offset0:128 offset1:160
	ds_read2_b32 v[12:13], v5 offset0:128 offset1:160
	s_waitcnt lgkmcnt(0)
	v_add3_u32 v16, v14, v12, v13
	ds_read2_b32 v[12:13], v4 offset0:192 offset1:224
	ds_read2_b32 v[14:15], v5 offset0:192 offset1:224
	s_waitcnt lgkmcnt(0)
	v_add3_u32 v5, v16, v14, v15
	ds_read2_b32 v[16:17], v23 offset1:32
	ds_read2_b32 v[14:15], v22 offset1:32
	s_waitcnt lgkmcnt(1)
	v_add3_u32 v5, v5, v16, v17
	ds_read2_b32 v[16:17], v22 offset0:64 offset1:96
	ds_read2_b32 v[18:19], v23 offset0:64 offset1:96
	s_waitcnt lgkmcnt(0)
	v_add3_u32 v5, v5, v18, v19
	ds_read2_b32 v[18:19], v22 offset0:128 offset1:160
	ds_read2_b32 v[20:21], v23 offset0:128 offset1:160
	s_waitcnt lgkmcnt(0)
	v_add3_u32 v5, v5, v20, v21
	ds_read2_b32 v[20:21], v22 offset0:192 offset1:224
	ds_read2_b32 v[22:23], v23 offset0:192 offset1:224
	s_waitcnt lgkmcnt(0)
	v_add3_u32 v5, v5, v22, v23
	v_add_u32_e32 v22, 0x24e00, v4
	ds_write_b32 v22, v5
	v_add3_u32 v5, v6, v7, v8
	v_add3_u32 v5, v5, v9, v10
	v_add3_u32 v5, v5, v11, v12
	v_add3_u32 v5, v5, v13, v14
	v_add3_u32 v5, v5, v15, v16
	v_add3_u32 v5, v5, v17, v18
	v_add3_u32 v5, v5, v19, v20
	v_add3_u32 v5, v5, v21, s3
	v_ashrrev_i32_e32 v6, 8, v5
	v_and_b32_e32 v5, 64, v249
	v_add_u32_e32 v7, -1, v249
	v_cmp_lt_i32_e64 s[38:39], v7, v5
	v_add_u32_e32 v8, -2, v249
	s_nop 0
	v_cndmask_b32_e64 v7, v7, v249, s[38:39]
	v_lshlrev_b32_e32 v7, 2, v7
	ds_bpermute_b32 v7, v7, v6
	v_cmp_lt_i32_e64 s[38:39], 0, v3
	s_waitcnt lgkmcnt(0)
	s_nop 0
	v_cndmask_b32_e64 v7, 0, v7, s[38:39]
	v_cmp_lt_i32_e64 s[38:39], v8, v5
	v_add_u32_e32 v7, v7, v6
	s_nop 0
	v_cndmask_b32_e64 v8, v8, v249, s[38:39]
	v_lshlrev_b32_e32 v8, 2, v8
	ds_bpermute_b32 v8, v8, v7
	v_cmp_lt_i32_e64 s[38:39], 1, v3
	s_waitcnt lgkmcnt(0)
	s_nop 0
	v_cndmask_b32_e64 v8, 0, v8, s[38:39]
	v_add_u32_e32 v7, v8, v7
	v_add_u32_e32 v8, -4, v249
	v_cmp_lt_i32_e64 s[38:39], v8, v5
	s_nop 1
	v_cndmask_b32_e64 v8, v8, v249, s[38:39]
	v_lshlrev_b32_e32 v8, 2, v8
	ds_bpermute_b32 v8, v8, v7
	v_cmp_lt_i32_e64 s[38:39], 3, v3
	s_waitcnt lgkmcnt(0)
	s_nop 0
	v_cndmask_b32_e64 v8, 0, v8, s[38:39]
	v_add_u32_e32 v7, v8, v7
	v_add_u32_e32 v8, -8, v249
	v_cmp_lt_i32_e64 s[38:39], v8, v5
	s_nop 1
	v_cndmask_b32_e64 v8, v8, v249, s[38:39]
	v_lshlrev_b32_e32 v8, 2, v8
	ds_bpermute_b32 v8, v8, v7
	v_cmp_lt_i32_e64 s[38:39], 7, v3
	s_waitcnt lgkmcnt(0)
	s_nop 0
	v_cndmask_b32_e64 v8, 0, v8, s[38:39]
	v_add_u32_e32 v7, v8, v7
	v_add_u32_e32 v8, -16, v249
	v_cmp_lt_i32_e64 s[38:39], v8, v5
	s_nop 1
	v_cndmask_b32_e64 v5, v8, v249, s[38:39]
	v_lshlrev_b32_e32 v5, 2, v5
	ds_bpermute_b32 v5, v5, v7
	v_cmp_lt_i32_e64 s[38:39], 15, v3
	s_waitcnt lgkmcnt(0)
	s_nop 0
	v_cndmask_b32_e64 v5, 0, v5, s[38:39]
	v_add_u32_e32 v5, v5, v7
	v_sub_u32_e32 v6, v5, v6
	v_add_u32_e32 v7, 0x24840, v4
	v_cmp_eq_u32_e64 s[38:39], 31, v3
	ds_write_b32 v7, v6
	s_and_b64 exec, exec, s[38:39]
	s_cbranch_execz .LBB0_1135
	v_readlane_b32 s3, v254, 33
	v_min_i32_e32 v6, 0xa0, v5
	s_nop 0
	v_mov_b32_e32 v7, s3
	v_readlane_b32 s3, v254, 34
	ds_write_b32 v7, v5
	s_nop 0
	v_mov_b32_e32 v5, s3
	ds_write_b32 v5, v6

.LBB0_1138:
	s_or_b64 exec, exec, s[36:37]
	s_waitcnt lgkmcnt(0)
	s_barrier
	s_and_saveexec_b64 s[26:27], vcc
	s_cbranch_execz .LBB0_1131
	v_ashrrev_i32_e32 v3, 31, v2
	v_lshlrev_b64 v[4:5], 2, v[2:3]
	v_lshl_add_u64 v[6:7], s[46:47], 0, v[4:5]
	v_mov_b32_e32 v3, v86
	v_lshl_add_u64 v[6:7], s[44:45], 0, v[4:5]
	v_mov_b32_e32 v6, v87
	v_lshl_add_u64 v[4:5], s[42:43], 0, v[4:5]
	v_ashrrev_i32_e32 v8, 1, v2
	s_waitcnt vmcnt(1)
	v_lshl_add_u32 v3, v3, 2, 0
	v_add_u32_e32 v7, 0x24840, v3
	v_add_u32_e32 v3, 0x24e00, v3
	ds_read_b32 v7, v7
	ds_read_b32 v3, v3
	s_waitcnt lgkmcnt(1)
	v_lshlrev_b32_e32 v7, 8, v7
	s_waitcnt vmcnt(0) lgkmcnt(0)
	v_add3_u32 v6, v7, v3, v6
	v_ashrrev_i32_e32 v7, 31, v6
	global_store_dword v[4:5], v6, off
	v_lshl_add_u64 v[4:5], v[6:7], 2, s[34:35]
	global_store_dword v[4:5], v8, off
	s_branch .LBB0_1131

.LBB0_1213:
	s_lshl_b32 s6, s7, 6
	s_and_b32 s6, s6, 0xffffff00
	v_add_u32_e32 v4, s6, v205
	v_ashrrev_i32_e32 v5, 31, v4
	v_lshl_add_u64 v[4:5], v[4:5], 2, s[36:37]
	global_load_dword v70, v[4:5], off
	s_add_i32 s6, s4, s87
	s_cmp_ge_i32 s6, s3
	s_cbranch_scc0 .LBB0_1216

.LBB0_1218:
	s_lshl_b32 s7, s8, 6
	s_and_b32 s7, s7, 0xffffff00
	v_add_u32_e32 v4, s7, v205
	v_ashrrev_i32_e32 v5, 31, v4
	v_lshl_add_u64 v[4:5], v[4:5], 2, s[36:37]
	global_load_dword v71, v[4:5], off
	s_add_i32 s6, s6, s4
	s_cmp_ge_i32 s6, s3
	s_cbranch_scc1 .LBB0_1222

.LBB0_1221:
	s_lshl_b32 s6, s6, 6
	s_and_b32 s6, s6, 0xffffff00
	v_add_u32_e32 v4, s6, v205
	v_ashrrev_i32_e32 v5, 31, v4
	v_lshl_add_u64 v[4:5], v[4:5], 2, s[36:37]
	global_load_dword v72, v[4:5], off
.LBB0_1222:
	s_waitcnt vmcnt(0)
	ds_write_b32 v2, v70
	ds_write_b32 v2, v71 offset:1024
	ds_write_b32 v2, v72 offset:2048
	v_mov_b32_e32 v230, s5
